# conversion-in-attention (12 units per wave, every 4th iteration) with a catch-up tail for grids with fewer loop trips
# baseline (speedup 1.0000x reference)
; #define LAS __attribute__((address_space(3)))
; __device__ __forceinline__ void lds_barrier() { asm volatile("s_waitcnt lgkmcnt(0)\n\ts_barrier" ::: "memory"); }
; __device__ __forceinline__ void phase_attn(Frame& F) {
;     ...
;         lds_barrier();
;         LAS unsigned char* kb = F.lds + buf * ABUF;
;         const bf16x8 q0 = qn0, q1 = qn1;
;         {
;             LAS unsigned char* ob = F.lds + (buf ^ 1) * ABUF;
; #pragma unroll
;             for (int jj = 0; jj < 4; ++jj) { const int ch = tid + 512 * jj, row = ch >> 3, c16 = ch & 7;
;                 *(LAS u32x4*)(ob + row * ATT_ROWB + c16 * 16) = kr[jj]; *(LAS u32x4*)(ob + ATT_VOFF + row * ATT_ROWB + c16 * 16) = vr[jj]; }
;         }
;         const AttnUnit nu = un;
;         un = attn_decode(x8 * PER_X + (jl + 2 * G8 < jlast ? jl + 2 * G8 : jlast)); attn_issue(qkv, un, tid, kr, vr);
;         { const char* qb = (const char*)qkv + (((size_t)nu.b * SEQ + nu.r) * NPROJ + nu.h * 64) * 2; const unsigned qo = __umul24((unsigned)(128 * nu.n + ql), (unsigned)nu.d * (NPROJ * 2)) + 16u * fq;
;           qn0 = *(const bf16x8*)(qb + qo); qn1 = *(const bf16x8*)(qb + qo + 64); }
;         const unsigned qrow = __umul24((unsigned)(128 * cu.n + ql), (unsigned)cu.d);
;         const float c1 = 0.125f * LOG2E;
;         const float nc2 = -__builtin_amdgcn_exp2f(-(float)(cu.h + 1)) * (float)cu.d * LOG2E;
;         const bool first = cu.n == 0;
;         f32x4 St[9];
;         const f32x4 eb = (f32x4){ef[0], ef[1], ef[2], ef[3]} * nc2;
;         float mx = -INFINITY;
;         bf16x8 kf[9][2];
; #pragma unroll
;         for (int T = 0; T < 9; ++T) { LAS unsigned char* ka = kb + (16 * (w + T) + fr) * ATT_ROWB + fq * 16; kf[T][0] = *(LAS bf16x8*)ka; kf[T][1] = *(LAS bf16x8*)(ka + 64); }
.Lcva_wd:
	v_mov_b64_e32 v[48:49], v[4:5]
	v_mov_b64_e32 v[46:47], v[2:3]
	v_mov_b64_e32 v[44:45], v[8:9]
	v_mov_b64_e32 v[42:43], v[6:7]
	s_lshl_b32 s65, 1, s35
	s_waitcnt lgkmcnt(0)
	s_barrier
	s_add_i32 s37, s30, 1
	v_cvt_f32_u32_e32 v54, s37
	v_cvt_f32_u32_e32 v55, s65
	v_add_u32_e32 v110, s85, v82
	v_add_u32_e32 v58, v110, v90
	v_exp_f32_e64 v54, -v54
	v_add_u32_e32 v66, v110, v91
	v_add_u32_e32 v74, v110, v92
	v_add_u32_e32 v111, v110, v93
	v_mul_f32_e32 v79, v55, v54
	ds_read_b128 v[54:57], v58
	ds_read_b128 v[58:61], v58 offset:64
	ds_read_b128 v[62:65], v66
	ds_read_b128 v[66:69], v66 offset:64
	ds_read_b128 v[70:73], v74
	ds_read_b128 v[74:77], v74 offset:64
	ds_read_b128 v[112:115], v111
	ds_read_b128 v[116:119], v111 offset:64
	v_add_u32_e32 v111, v110, v94
	ds_read_b128 v[120:123], v111
	ds_read_b128 v[124:127], v111 offset:64
	v_add_u32_e32 v111, v110, v95
	ds_read_b128 v[128:131], v111
	ds_read_b128 v[132:135], v111 offset:64
	v_add_u32_e32 v111, v110, v96
	ds_read_b128 v[136:139], v111
	ds_read_b128 v[140:143], v111 offset:64
	v_add_u32_e32 v111, v110, v97
	v_add_u32_e32 v110, v110, v98
	ds_read_b128 v[144:147], v111
	ds_read_b128 v[148:151], v111 offset:64
	ds_read_b128 v[152:155], v110
	ds_read_b128 v[156:159], v110 offset:64
	s_sub_u32 s32, s32, 1
	s_cmp_lt_i32 s32, 0
	s_cbranch_scc0 .Lcva_none_l
	s_mov_b32 s32, 3
	s_cmp_eq_u32 s90, 0
	s_cbranch_scc1 .Lcva_none_l
	s_sub_u32 s90, s90, 1
	s_lshr_b32 s98, s89, 6
	s_and_b32 s99, s89, 63
	s_mul_hi_u32 s100, s98, 0xaaaaaaab
	s_lshr_b32 s100, s100, 1
	s_mul_i32 s101, s100, 3
	s_sub_u32 s101, s98, s101
	s_cmp_lt_u32 s100, 256
	s_cselect_b32 s98, 0, 3
	s_cselect_b32 s95, s100, 0
	s_add_u32 s98, s98, s101
	s_lshl_b32 s98, s98, 1
	v_readlane_b32 s96, v253, s98
	s_add_u32 s98, s98, 1
	v_readlane_b32 s97, v253, s98
	s_lshl_b32 s95, s95, 20
	s_nop 3
	s_add_u32 s96, s96, s95
	s_addc_u32 s97, s97, 0
	s_cmp_eq_u32 s101, 2
	s_cbranch_scc1 .Lcva_down_l
	s_lshr_b32 s95, s99, 3
	s_and_b32 s99, s99, 7
	s_lshl_b32 s98, s95, 17
	s_add_u32 s96, s96, s98
	s_addc_u32 s97, s97, 0
	s_lshl_b32 s98, s99, 7
	s_add_u32 s96, s96, s98
	s_addc_u32 s97, s97, 0
	s_lshl_b32 s100, s100, 19
	s_lshr_b32 s98, s99, 2
	s_lshl_b32 s98, s98, 18
	s_add_u32 s100, s100, s98
	s_and_b32 s98, s99, 3
	s_lshl_b32 s98, s98, 15
	s_add_u32 s100, s100, s98
	s_lshl_b32 s98, s101, 17
	s_add_u32 s100, s100, s98
	s_lshl_b32 s98, s95, 7
	s_add_u32 s100, s100, s98
	v_readlane_b32 s92, v253, 12
	v_readlane_b32 s93, v253, 13
	s_mov_b32 s94, 0xc3317218
	s_cmp_eq_u32 s101, 0
	s_cselect_b32 s94, 0xc2b8aa3b, s94
	s_nop 3
	s_add_u32 s92, s92, s100
	s_addc_u32 s93, s93, 0
	s_movk_i32 s95, 0x400
	s_movk_i32 s98, 0x400
	s_branch .Lcva_go_l

; __device__ __forceinline__ void convert_experts(Frame& F, int lo, int hi) {
;     ...
;         for (;;) {
;             const bool more = sq + 1 < ns; const int rn = more ? CONV_RIDX(sq + 1) : r;
;             if (more) { CONV_DESC(rn, tn); titem_issue(tn, F.lane, scr + (p ^ 1) * 8192); }
;             if (!more) asm volatile("s_waitcnt vmcnt(0)" ::: "memory");
;             else if (first) asm volatile("s_waitcnt vmcnt(8)" ::: "memory");
;             else asm volatile("s_waitcnt vmcnt(12)" ::: "memory");
;             titem_finish(tc, F.lane, scr + p * 8192);
;             asm volatile("s_waitcnt lgkmcnt(0)" ::: "memory");
;             if (!more) break;
;             tc = tn; r = rn; ++sq; p ^= 1; first = false;
.Lcva_tail:
	s_cmp_eq_u32 s90, 0
	s_cbranch_scc1 .Lcva_tail_done
	s_mov_b32 s32, 0
	s_mov_b32 s95, 0
	s_sub_u32 s32, s32, 1
	s_cmp_lt_i32 s32, 0
	s_cbranch_scc0 .Lcva_none_t
	s_mov_b32 s32, 3
	s_cmp_eq_u32 s90, 0
	s_cbranch_scc1 .Lcva_none_t
	s_sub_u32 s90, s90, 1
	s_lshr_b32 s98, s89, 6
	s_and_b32 s99, s89, 63
	s_mul_hi_u32 s100, s98, 0xaaaaaaab
	s_lshr_b32 s100, s100, 1
	s_mul_i32 s101, s100, 3
	s_sub_u32 s101, s98, s101
	s_cmp_lt_u32 s100, 256
	s_cselect_b32 s98, 0, 3
	s_cselect_b32 s95, s100, 0
	s_add_u32 s98, s98, s101
	s_lshl_b32 s98, s98, 1
	v_readlane_b32 s96, v253, s98
	s_add_u32 s98, s98, 1
	v_readlane_b32 s97, v253, s98
	s_lshl_b32 s95, s95, 20
	s_nop 3
	s_add_u32 s96, s96, s95
	s_addc_u32 s97, s97, 0
	s_cmp_eq_u32 s101, 2
	s_cbranch_scc1 .Lcva_down_t
	s_lshr_b32 s95, s99, 3
	s_and_b32 s99, s99, 7
	s_lshl_b32 s98, s95, 17
	s_add_u32 s96, s96, s98
	s_addc_u32 s97, s97, 0
	s_lshl_b32 s98, s99, 7
	s_add_u32 s96, s96, s98
	s_addc_u32 s97, s97, 0
	s_lshl_b32 s100, s100, 19
	s_lshr_b32 s98, s99, 2
	s_lshl_b32 s98, s98, 18
	s_add_u32 s100, s100, s98
	s_and_b32 s98, s99, 3
	s_lshl_b32 s98, s98, 15
	s_add_u32 s100, s100, s98
	s_lshl_b32 s98, s101, 17
	s_add_u32 s100, s100, s98
	s_lshl_b32 s98, s95, 7
	s_add_u32 s100, s100, s98
	v_readlane_b32 s92, v253, 12
	v_readlane_b32 s93, v253, 13
	s_mov_b32 s94, 0xc3317218
	s_cmp_eq_u32 s101, 0
	s_cselect_b32 s94, 0xc2b8aa3b, s94
	s_nop 3
	s_add_u32 s92, s92, s100
	s_addc_u32 s93, s93, 0
	s_movk_i32 s95, 0x400
	s_movk_i32 s98, 0x400
	s_branch .Lcva_go_t

; __device__ __forceinline__ void titem_finish(const TItem& t, int lane, const LAS unsigned char* buf) {
;     ...
;     if (t.f8) {
; #pragma unroll
;         for (int j = 0; j < 4; ++j) { const int n = (lane >> 3) + 8 * j;
;             int w0 = __builtin_amdgcn_cvt_pk_fp8_f32(v[j][0], v[j][1], 0, false); w0 = __builtin_amdgcn_cvt_pk_fp8_f32(v[j][2], v[j][3], w0, true);
;             int w1 = __builtin_amdgcn_cvt_pk_fp8_f32(v[j][4], v[j][5], 0, false); w1 = __builtin_amdgcn_cvt_pk_fp8_f32(v[j][6], v[j][7], w1, true);
;             u32x2 o; o.x = (unsigned)w0; o.y = (unsigned)w1;
;             __builtin_nontemporal_store(o, (u32x2*)((unsigned char*)t.WT + (size_t)(d0 + n) * t.K + k0 + 8 * c)); }
.Lcva_none_t:
	s_waitcnt vmcnt(0)
	s_cmp_eq_u32 s95, 0
	s_cbranch_scc1 .Lcva_skip_t
	s_waitcnt vmcnt(0)
	v_pk_mul_f32 v[168:169], v[168:169], s[94:95] op_sel_hi:[1,0]
	v_pk_mul_f32 v[170:171], v[170:171], s[94:95] op_sel_hi:[1,0]
	v_pk_mul_f32 v[172:173], v[172:173], s[94:95] op_sel_hi:[1,0]
	v_pk_mul_f32 v[174:175], v[174:175], s[94:95] op_sel_hi:[1,0]
	v_pk_mul_f32 v[176:177], v[176:177], s[94:95] op_sel_hi:[1,0]
	v_pk_mul_f32 v[178:179], v[178:179], s[94:95] op_sel_hi:[1,0]
	v_pk_mul_f32 v[180:181], v[180:181], s[94:95] op_sel_hi:[1,0]
	v_pk_mul_f32 v[182:183], v[182:183], s[94:95] op_sel_hi:[1,0]
	v_pk_mul_f32 v[184:185], v[184:185], s[94:95] op_sel_hi:[1,0]
	v_pk_mul_f32 v[186:187], v[186:187], s[94:95] op_sel_hi:[1,0]
	v_pk_mul_f32 v[188:189], v[188:189], s[94:95] op_sel_hi:[1,0]
	v_pk_mul_f32 v[190:191], v[190:191], s[94:95] op_sel_hi:[1,0]
	v_pk_mul_f32 v[192:193], v[192:193], s[94:95] op_sel_hi:[1,0]
	v_pk_mul_f32 v[194:195], v[194:195], s[94:95] op_sel_hi:[1,0]
	v_pk_mul_f32 v[196:197], v[196:197], s[94:95] op_sel_hi:[1,0]
	v_pk_mul_f32 v[198:199], v[198:199], s[94:95] op_sel_hi:[1,0]
	v_pk_mul_f32 v[200:201], v[200:201], s[94:95] op_sel_hi:[1,0]
	v_pk_mul_f32 v[202:203], v[202:203], s[94:95] op_sel_hi:[1,0]
	v_pk_mul_f32 v[204:205], v[204:205], s[94:95] op_sel_hi:[1,0]
	v_pk_mul_f32 v[206:207], v[206:207], s[94:95] op_sel_hi:[1,0]
	v_pk_mul_f32 v[208:209], v[208:209], s[94:95] op_sel_hi:[1,0]
	v_pk_mul_f32 v[210:211], v[210:211], s[94:95] op_sel_hi:[1,0]
	v_pk_mul_f32 v[212:213], v[212:213], s[94:95] op_sel_hi:[1,0]
	v_pk_mul_f32 v[214:215], v[214:215], s[94:95] op_sel_hi:[1,0]
	v_pk_mul_f32 v[216:217], v[216:217], s[94:95] op_sel_hi:[1,0]
	v_pk_mul_f32 v[218:219], v[218:219], s[94:95] op_sel_hi:[1,0]
	v_pk_mul_f32 v[220:221], v[220:221], s[94:95] op_sel_hi:[1,0]
	v_pk_mul_f32 v[222:223], v[222:223], s[94:95] op_sel_hi:[1,0]
	v_pk_mul_f32 v[224:225], v[224:225], s[94:95] op_sel_hi:[1,0]
	v_pk_mul_f32 v[226:227], v[226:227], s[94:95] op_sel_hi:[1,0]
	v_pk_mul_f32 v[228:229], v[228:229], s[94:95] op_sel_hi:[1,0]
	v_pk_mul_f32 v[230:231], v[230:231], s[94:95] op_sel_hi:[1,0]
	s_lshr_b32 s99, s95, 2
	v_lshlrev_b32_e32 v250, 4, v248
	v_cvt_pk_fp8_f32 v232, v168, v172
	v_cvt_pk_fp8_f32 v233, v184, v188
	v_cvt_pk_fp8_f32 v234, v200, v204
	v_cvt_pk_fp8_f32 v235, v216, v220
	v_cvt_pk_fp8_f32 v236, v169, v173
	v_cvt_pk_fp8_f32 v237, v185, v189
	v_cvt_pk_fp8_f32 v238, v201, v205
	v_cvt_pk_fp8_f32 v239, v217, v221
	v_cvt_pk_fp8_f32 v240, v170, v174
	v_cvt_pk_fp8_f32 v241, v186, v190
	v_cvt_pk_fp8_f32 v242, v202, v206
	v_cvt_pk_fp8_f32 v243, v218, v222
	v_cvt_pk_fp8_f32 v244, v171, v175
	v_cvt_pk_fp8_f32 v245, v187, v191
	v_cvt_pk_fp8_f32 v246, v203, v207
	v_cvt_pk_fp8_f32 v247, v219, v223
	v_mad_u32_u24 v250, v249, s99, v250
	v_add_u32_e32 v251, s95, v250
	v_add_u32_e32 v254, s95, v251
	v_add_u32_e32 v255, s95, v254
	v_cvt_pk_fp8_f32 v232, v176, v180 op_sel:[0,0,1]
	v_cvt_pk_fp8_f32 v233, v192, v196 op_sel:[0,0,1]
	v_cvt_pk_fp8_f32 v234, v208, v212 op_sel:[0,0,1]
	v_cvt_pk_fp8_f32 v235, v224, v228 op_sel:[0,0,1]
	v_cvt_pk_fp8_f32 v236, v177, v181 op_sel:[0,0,1]
	v_cvt_pk_fp8_f32 v237, v193, v197 op_sel:[0,0,1]
	v_cvt_pk_fp8_f32 v238, v209, v213 op_sel:[0,0,1]
	v_cvt_pk_fp8_f32 v239, v225, v229 op_sel:[0,0,1]
	v_cvt_pk_fp8_f32 v240, v178, v182 op_sel:[0,0,1]
	v_cvt_pk_fp8_f32 v241, v194, v198 op_sel:[0,0,1]
	v_cvt_pk_fp8_f32 v242, v210, v214 op_sel:[0,0,1]
	v_cvt_pk_fp8_f32 v243, v226, v230 op_sel:[0,0,1]
	v_cvt_pk_fp8_f32 v244, v179, v183 op_sel:[0,0,1]
	v_cvt_pk_fp8_f32 v245, v195, v199 op_sel:[0,0,1]
	v_cvt_pk_fp8_f32 v246, v211, v215 op_sel:[0,0,1]
	v_cvt_pk_fp8_f32 v247, v227, v231 op_sel:[0,0,1]
	global_store_dwordx4 v250, v[232:235], s[92:93] nt
	global_store_dwordx4 v251, v[236:239], s[92:93] nt
	global_store_dwordx4 v254, v[240:243], s[92:93] nt
	global_store_dwordx4 v255, v[244:247], s[92:93] nt
.Lcva_skip_t:
	s_waitcnt vmcnt(0)
	s_branch .Lcva_tail
